# P0 expert conversion: the per-tile work-counter atomic returns into its own VGPR and is no longer followed by a vmcnt(0) drain (its value is first read behind a later full wait)
# speedup vs baseline: 1.0115x; 1.0115x over previous
.LBB0_176:
	v_mov_b32_e32 v66, v0
	v_mov_b32_e32 v224, 0
	v_and_b32_e32 v66, 63, v66
	v_cmp_eq_u32_e32 vcc, 0, v66
	s_and_saveexec_b64 s[4:5], vcc
	s_cbranch_execz .LBB0_180
	s_mov_b64 s[22:23], exec
	v_mbcnt_lo_u32_b32 v66, s22, 0
	v_mbcnt_hi_u32_b32 v66, s23, v66
	v_cmp_eq_u32_e32 vcc, 0, v66
	s_and_saveexec_b64 s[6:7], vcc
	s_cbranch_execz .LBB0_179
	s_bcnt1_i32_b64 s22, s[22:23]
	v_mov_b32_e32 v67, s22
	global_atomic_add v224, v131, v67, s[68:69] offset:256 sc0
.LBB0_179:
	s_or_b64 exec, exec, s[6:7]
.LBB0_180:
	s_or_b64 exec, exec, s[4:5]
	s_lshl_b32 s5, s30, 7
	v_or_b32_e32 v84, s5, v1
	v_or_b32_e32 v82, 0x60, v84
	v_mad_u64_u32 v[82:83], s[6:7], v82, s27, 0
	v_lshl_add_u64 v[82:83], v[82:83], 2, s[18:19]
	v_lshl_add_u64 v[152:153], v[82:83], 0, v[130:131]
	v_or_b32_e32 v82, 0x61, v84
	v_mad_u64_u32 v[82:83], s[6:7], v82, s27, 0
	v_lshl_add_u64 v[82:83], v[82:83], 2, s[18:19]
	v_lshl_add_u64 v[154:155], v[82:83], 0, v[130:131]
	v_or_b32_e32 v82, 0x62, v84
	v_mad_u64_u32 v[82:83], s[6:7], v82, s27, 0
	v_lshl_add_u64 v[82:83], v[82:83], 2, s[18:19]
	v_lshl_add_u64 v[156:157], v[82:83], 0, v[130:131]
	v_or_b32_e32 v82, 0x63, v84
	v_mad_u64_u32 v[82:83], s[6:7], v82, s27, 0
	v_lshl_add_u64 v[82:83], v[82:83], 2, s[18:19]
	v_lshl_add_u64 v[158:159], v[82:83], 0, v[130:131]
	v_or_b32_e32 v82, 0x64, v84
	v_mad_u64_u32 v[82:83], s[6:7], v82, s27, 0
	v_lshl_add_u64 v[82:83], v[82:83], 2, s[18:19]
	v_lshl_add_u64 v[160:161], v[82:83], 0, v[130:131]
	v_or_b32_e32 v82, 0x65, v84
	v_mad_u64_u32 v[82:83], s[6:7], v82, s27, 0
	v_lshl_add_u64 v[82:83], v[82:83], 2, s[18:19]
	v_lshl_add_u64 v[162:163], v[82:83], 0, v[130:131]
	v_or_b32_e32 v82, 0x66, v84
	v_mad_u64_u32 v[82:83], s[6:7], v82, s27, 0
	v_lshl_add_u64 v[82:83], v[82:83], 2, s[18:19]
	s_and_b32 s4, s8, 15
	s_lshl_b32 s8, s29, 8
	v_or_b32_e32 v66, 64, v84
	v_or_b32_e32 v68, 0x41, v84
	v_or_b32_e32 v70, 0x42, v84
	v_or_b32_e32 v72, 0x43, v84
	v_or_b32_e32 v74, 0x44, v84
	v_or_b32_e32 v76, 0x45, v84
	v_or_b32_e32 v78, 0x46, v84
	v_or_b32_e32 v80, 0x47, v84
	v_lshl_add_u64 v[106:107], v[82:83], 0, v[130:131]
	v_or_b32_e32 v82, 0x67, v84
	v_mad_u64_u32 v[66:67], s[6:7], v66, s27, 0
	v_mad_u64_u32 v[68:69], s[6:7], v68, s27, 0
	v_mad_u64_u32 v[70:71], s[6:7], v70, s27, 0
	v_mad_u64_u32 v[72:73], s[6:7], v72, s27, 0
	v_mad_u64_u32 v[74:75], s[6:7], v74, s27, 0
	v_mad_u64_u32 v[76:77], s[6:7], v76, s27, 0
	v_mad_u64_u32 v[78:79], s[6:7], v78, s27, 0
	v_mad_u64_u32 v[80:81], s[6:7], v80, s27, 0
	v_mad_u64_u32 v[82:83], s[6:7], v82, s27, 0
	s_cmp_eq_u32 s28, 0
	s_cselect_b64 s[6:7], -1, 0
	s_add_u32 s20, s20, s5
	v_lshl_add_u64 v[82:83], v[82:83], 2, s[18:19]
	s_addc_u32 s21, s21, 0
	v_lshl_add_u64 v[108:109], v[82:83], 0, v[130:131]
	v_lshl_add_u64 v[134:135], s[20:21], 0, v[132:133]
	v_mad_u64_u32 v[82:83], s[20:21], v84, s27, 0
	v_lshl_add_u64 v[82:83], v[82:83], 2, s[18:19]
	v_lshl_add_u64 v[110:111], v[82:83], 0, v[130:131]
	v_or_b32_e32 v82, 1, v84
	v_mad_u64_u32 v[82:83], s[20:21], v82, s27, 0
	v_lshl_add_u64 v[82:83], v[82:83], 2, s[18:19]
	v_lshl_add_u64 v[112:113], v[82:83], 0, v[130:131]
	v_or_b32_e32 v82, 2, v84
	v_mad_u64_u32 v[82:83], s[20:21], v82, s27, 0
	v_lshl_add_u64 v[82:83], v[82:83], 2, s[18:19]
	v_lshl_add_u64 v[114:115], v[82:83], 0, v[130:131]
	v_or_b32_e32 v82, 3, v84
	v_mad_u64_u32 v[82:83], s[20:21], v82, s27, 0
	v_lshl_add_u64 v[82:83], v[82:83], 2, s[18:19]
	v_lshl_add_u64 v[116:117], v[82:83], 0, v[130:131]
	v_or_b32_e32 v82, 4, v84
	v_mad_u64_u32 v[82:83], s[20:21], v82, s27, 0
	v_lshl_add_u64 v[82:83], v[82:83], 2, s[18:19]
	v_lshl_add_u64 v[118:119], v[82:83], 0, v[130:131]
	v_or_b32_e32 v82, 5, v84
	v_mad_u64_u32 v[82:83], s[20:21], v82, s27, 0
	v_lshl_add_u64 v[82:83], v[82:83], 2, s[18:19]
	v_lshl_add_u64 v[120:121], v[82:83], 0, v[130:131]
	v_or_b32_e32 v82, 6, v84
	v_mad_u64_u32 v[82:83], s[20:21], v82, s27, 0
	v_lshl_add_u64 v[82:83], v[82:83], 2, s[18:19]
	v_lshl_add_u64 v[122:123], v[82:83], 0, v[130:131]
	v_or_b32_e32 v82, 7, v84
	v_mad_u64_u32 v[82:83], s[20:21], v82, s27, 0
	v_lshl_add_u64 v[82:83], v[82:83], 2, s[18:19]
	v_lshl_add_u64 v[124:125], v[82:83], 0, v[130:131]
	v_or_b32_e32 v82, 32, v84
	v_mad_u64_u32 v[82:83], s[20:21], v82, s27, 0
	v_lshl_add_u64 v[82:83], v[82:83], 2, s[18:19]
	v_lshl_add_u64 v[126:127], v[82:83], 0, v[130:131]
	v_or_b32_e32 v82, 33, v84
	v_mad_u64_u32 v[82:83], s[20:21], v82, s27, 0
	v_lshl_add_u64 v[82:83], v[82:83], 2, s[18:19]
	v_lshl_add_u64 v[128:129], v[82:83], 0, v[130:131]
	v_or_b32_e32 v82, 34, v84
	v_mad_u64_u32 v[82:83], s[20:21], v82, s27, 0
	v_lshl_add_u64 v[82:83], v[82:83], 2, s[18:19]
	v_lshl_add_u64 v[178:179], v[82:83], 0, v[130:131]
	v_or_b32_e32 v82, 35, v84
	v_mad_u64_u32 v[82:83], s[20:21], v82, s27, 0
	v_lshl_add_u64 v[82:83], v[82:83], 2, s[18:19]
	v_lshl_add_u64 v[176:177], v[82:83], 0, v[130:131]
	v_or_b32_e32 v82, 36, v84
	v_mad_u64_u32 v[82:83], s[20:21], v82, s27, 0
	v_lshl_add_u64 v[82:83], v[82:83], 2, s[18:19]
	v_lshl_add_u64 v[174:175], v[82:83], 0, v[130:131]
	v_or_b32_e32 v82, 37, v84
	v_mad_u64_u32 v[82:83], s[20:21], v82, s27, 0
	v_lshl_add_u64 v[82:83], v[82:83], 2, s[18:19]
	v_lshl_add_u64 v[172:173], v[82:83], 0, v[130:131]
	v_or_b32_e32 v82, 38, v84
	v_mad_u64_u32 v[82:83], s[20:21], v82, s27, 0
	v_lshl_add_u64 v[82:83], v[82:83], 2, s[18:19]
	v_lshl_add_u64 v[170:171], v[82:83], 0, v[130:131]
	v_or_b32_e32 v82, 39, v84
	v_lshl_add_u64 v[66:67], v[66:67], 2, s[18:19]
	v_mad_u64_u32 v[82:83], s[20:21], v82, s27, 0
	v_lshl_add_u64 v[66:67], v[66:67], 0, v[130:131]
	v_lshl_add_u64 v[68:69], v[68:69], 2, s[18:19]
	v_lshl_add_u64 v[70:71], v[70:71], 2, s[18:19]
	v_lshl_add_u64 v[72:73], v[72:73], 2, s[18:19]
	v_lshl_add_u64 v[74:75], v[74:75], 2, s[18:19]
	v_lshl_add_u64 v[76:77], v[76:77], 2, s[18:19]
	v_lshl_add_u64 v[78:79], v[78:79], 2, s[18:19]
	v_lshl_add_u64 v[80:81], v[80:81], 2, s[18:19]
	v_lshl_add_u64 v[82:83], v[82:83], 2, s[18:19]
	s_lshl_b64 s[18:19], s[8:9], 2
	v_lshl_add_u64 v[68:69], v[68:69], 0, v[130:131]
	v_lshl_add_u64 v[70:71], v[70:71], 0, v[130:131]
	v_lshl_add_u64 v[74:75], v[74:75], 0, v[130:131]
	v_lshl_add_u64 v[136:137], v[66:67], 0, s[18:19]
	v_lshl_add_u64 v[72:73], v[72:73], 0, v[130:131]
	v_lshl_add_u64 v[76:77], v[76:77], 0, v[130:131]
	v_lshl_add_u64 v[138:139], v[68:69], 0, s[18:19]
	global_load_dwordx4 v[98:101], v[136:137], off nt
	global_load_dwordx4 v[102:105], v[138:139], off nt
	v_lshl_add_u64 v[140:141], v[70:71], 0, s[18:19]
	v_lshl_add_u64 v[144:145], v[74:75], 0, s[18:19]
	v_lshl_add_u64 v[168:169], v[82:83], 0, v[130:131]
	v_lshl_add_u64 v[142:143], v[72:73], 0, s[18:19]
	global_load_dwordx4 v[94:97], v[140:141], off nt
	global_load_dwordx4 v[90:93], v[142:143], off nt
	v_lshl_add_u64 v[146:147], v[76:77], 0, s[18:19]
	global_load_dwordx4 v[86:89], v[144:145], off nt
	global_load_dwordx4 v[82:85], v[146:147], off nt
	v_lshl_add_u64 v[78:79], v[78:79], 0, v[130:131]
	v_lshl_add_u64 v[80:81], v[80:81], 0, v[130:131]
	v_lshl_add_u64 v[148:149], v[78:79], 0, s[18:19]
	v_lshl_add_u64 v[150:151], v[80:81], 0, s[18:19]
	global_load_dwordx4 v[74:77], v[148:149], off nt
	global_load_dwordx4 v[78:81], v[150:151], off nt
	s_waitcnt vmcnt(23)
	v_mul_f32_e32 v181, 0x42800000, v58
	s_waitcnt vmcnt(22)
	v_mul_f32_e32 v182, 0x42800000, v62
	v_mov_b32_e32 v180, v131
	v_cvt_pk_fp8_f32 v180, v181, v182
	s_waitcnt vmcnt(19)
	v_mul_f32_e32 v54, 0x42800000, v54
	s_waitcnt vmcnt(18)
	v_mul_f32_e32 v34, 0x42800000, v34
	v_mov_b32_e32 v181, v131
	v_cvt_pk_fp8_f32 v181, v54, v34
	v_mul_f32_e32 v34, 0x42800000, v50
	v_mul_f32_e32 v42, 0x42800000, v42
	v_cvt_pk_fp8_f32 v180, v34, v42 op_sel:[0,0,1]
	s_waitcnt vmcnt(17)
	v_mul_f32_e32 v34, 0x42800000, v38
	s_waitcnt vmcnt(16)
	v_mul_f32_e32 v38, 0x42800000, v46
	v_mul_f32_e32 v183, 0x42800000, v59
	v_mul_f32_e32 v184, 0x42800000, v63
	v_cvt_pk_fp8_f32 v181, v34, v38 op_sel:[0,0,1]
	v_mov_b32_e32 v34, v131
	v_cvt_pk_fp8_f32 v34, v183, v184
	v_mul_f32_e32 v38, 0x42800000, v55
	v_mul_f32_e32 v42, 0x42800000, v35
	v_mov_b32_e32 v35, v131
	v_cvt_pk_fp8_f32 v35, v38, v42
	v_mul_f32_e32 v38, 0x42800000, v51
	v_mul_f32_e32 v42, 0x42800000, v43
	v_cvt_pk_fp8_f32 v34, v38, v42 op_sel:[0,0,1]
	v_mul_f32_e32 v38, 0x42800000, v39
	v_mul_f32_e32 v39, 0x42800000, v47
	v_lshl_add_u64 v[152:153], v[152:153], 0, s[18:19]
	v_cvt_pk_fp8_f32 v35, v38, v39 op_sel:[0,0,1]
	v_mul_f32_e32 v42, 0x42800000, v56
	v_mul_f32_e32 v36, 0x42800000, v36
	v_mov_b32_e32 v39, v131
	v_lshl_add_u64 v[154:155], v[154:155], 0, s[18:19]
	global_load_dwordx4 v[66:69], v[152:153], off nt
	global_load_dwordx4 v[70:73], v[154:155], off nt
	v_lshl_add_u64 v[156:157], v[156:157], 0, s[18:19]
	v_mul_f32_e32 v185, 0x42800000, v60
	v_mul_f32_e32 v186, 0x42800000, v64
	v_lshl_add_u64 v[164:165], v[160:161], 0, s[18:19]
	v_mov_b32_e32 v38, v131
	v_cvt_pk_fp8_f32 v39, v42, v36
	v_lshl_add_u64 v[158:159], v[158:159], 0, s[18:19]
	v_mul_f32_e32 v187, 0x42800000, v61
	v_mul_f32_e32 v188, 0x42800000, v65
	global_load_dwordx4 v[58:61], v[156:157], off nt
	global_load_dwordx4 v[62:65], v[158:159], off nt
	v_lshl_add_u64 v[166:167], v[162:163], 0, s[18:19]
	v_mul_f32_e32 v46, 0x42800000, v52
	v_mul_f32_e32 v47, 0x42800000, v53
	v_mul_f32_e32 v54, 0x42800000, v44
	v_mul_f32_e32 v182, 0x42800000, v45
	v_cvt_pk_fp8_f32 v38, v185, v186
	global_load_dwordx4 v[42:45], v[164:165], off nt
	global_load_dwordx4 v[50:53], v[166:167], off nt
	v_mul_f32_e32 v56, 0x42800000, v37
	v_mul_f32_e32 v36, 0x42800000, v40
	v_mul_f32_e32 v37, 0x42800000, v48
	v_mul_f32_e32 v55, 0x42800000, v57
	v_lshl_add_u64 v[160:161], v[106:107], 0, s[18:19]
	v_cvt_pk_fp8_f32 v39, v36, v37 op_sel:[0,0,1]
	v_mov_b32_e32 v37, v131
	v_lshl_add_u64 v[162:163], v[108:109], 0, s[18:19]
	v_cvt_pk_fp8_f32 v38, v46, v54 op_sel:[0,0,1]
	v_cvt_pk_fp8_f32 v37, v55, v56
	global_load_dwordx4 v[54:57], v[160:161], off nt
	global_load_dwordx4 v[106:109], v[162:163], off nt
	v_mov_b32_e32 v36, v131
	v_cvt_pk_fp8_f32 v36, v187, v188
	v_mul_f32_e32 v40, 0x42800000, v41
	v_mul_f32_e32 v41, 0x42800000, v49
	v_cvt_pk_fp8_f32 v37, v40, v41 op_sel:[0,0,1]
	v_cvt_pk_fp8_f32 v36, v47, v182 op_sel:[0,0,1]
	ds_write_b64 v236, v[180:181]
	ds_write_b64 v236, v[34:35] offset:128
	ds_write_b64 v236, v[38:39] offset:256
	ds_write_b64 v236, v[36:37] offset:384
	s_waitcnt vmcnt(23)
	v_mul_f32_e32 v2, 0x42800000, v2
	s_waitcnt vmcnt(22)
	v_mul_f32_e32 v6, 0x42800000, v6
	v_mov_b32_e32 v34, v131
	v_cvt_pk_fp8_f32 v34, v2, v6
	s_waitcnt vmcnt(19)
	v_mul_f32_e32 v2, 0x42800000, v18
	s_waitcnt vmcnt(18)
	v_mul_f32_e32 v6, 0x42800000, v22
	v_mov_b32_e32 v35, v131
	v_cvt_pk_fp8_f32 v35, v2, v6
	s_waitcnt vmcnt(17)
	v_mul_f32_e32 v2, 0x42800000, v26
	s_waitcnt vmcnt(16)
	v_mul_f32_e32 v6, 0x42800000, v30
	v_mul_f32_e32 v3, 0x42800000, v3
	v_cvt_pk_fp8_f32 v35, v2, v6 op_sel:[0,0,1]
	v_mul_f32_e32 v6, 0x42800000, v7
	v_mov_b32_e32 v2, v131
	v_mul_f32_e32 v7, 0x42800000, v11
	v_cvt_pk_fp8_f32 v2, v3, v6
	v_mul_f32_e32 v6, 0x42800000, v19
	v_mul_f32_e32 v11, 0x42800000, v23
	v_mov_b32_e32 v3, v131
	v_cvt_pk_fp8_f32 v3, v6, v11
	v_mul_f32_e32 v10, 0x42800000, v10
	v_mul_f32_e32 v14, 0x42800000, v14
	v_cvt_pk_fp8_f32 v34, v10, v14 op_sel:[0,0,1]
	v_mul_f32_e32 v10, 0x42800000, v15
	v_cvt_pk_fp8_f32 v2, v7, v10 op_sel:[0,0,1]
	v_mul_f32_e32 v6, 0x42800000, v27
	v_mul_f32_e32 v7, 0x42800000, v31
	v_cvt_pk_fp8_f32 v3, v6, v7 op_sel:[0,0,1]
	v_mul_f32_e32 v4, 0x42800000, v4
	v_mul_f32_e32 v7, 0x42800000, v8
	v_mov_b32_e32 v6, v131
	s_waitcnt vmcnt(15)
	v_mul_f32_e32 v47, 0x42800000, v98
	s_waitcnt vmcnt(14)
	v_mul_f32_e32 v48, 0x42800000, v102
	v_mov_b32_e32 v46, v131
	v_cvt_pk_fp8_f32 v6, v4, v7
	v_mul_f32_e32 v4, 0x42800000, v20
	v_mul_f32_e32 v11, 0x42800000, v24
	v_mov_b32_e32 v7, v131
	v_cvt_pk_fp8_f32 v46, v47, v48
	s_waitcnt vmcnt(11)
	v_mul_f32_e32 v48, 0x42800000, v86
	s_waitcnt vmcnt(10)
	v_mul_f32_e32 v82, 0x42800000, v82
	v_mov_b32_e32 v47, v131
	v_cvt_pk_fp8_f32 v7, v4, v11
	v_cvt_pk_fp8_f32 v47, v48, v82
	v_mul_f32_e32 v8, 0x42800000, v12
	v_mul_f32_e32 v10, 0x42800000, v16
	v_mul_f32_e32 v48, 0x42800000, v94
	v_mul_f32_e32 v82, 0x42800000, v90
	v_cvt_pk_fp8_f32 v6, v8, v10 op_sel:[0,0,1]
	v_mul_f32_e32 v4, 0x42800000, v28
	v_mul_f32_e32 v8, 0x42800000, v32
	v_cvt_pk_fp8_f32 v46, v48, v82 op_sel:[0,0,1]
	s_waitcnt vmcnt(9)
	v_mul_f32_e32 v48, 0x42800000, v74
	s_waitcnt vmcnt(8)
	v_mul_f32_e32 v74, 0x42800000, v78
	v_cvt_pk_fp8_f32 v7, v4, v8 op_sel:[0,0,1]
	v_mul_f32_e32 v5, 0x42800000, v5
	v_mul_f32_e32 v8, 0x42800000, v9
	v_mov_b32_e32 v4, v131
	v_lshl_add_u64 v[190:191], v[118:119], 0, s[18:19]
	v_mul_f32_e32 v49, 0x42800000, v99
	v_mul_f32_e32 v118, 0x42800000, v103
	v_cvt_pk_fp8_f32 v47, v48, v74 op_sel:[0,0,1]
	v_mov_b32_e32 v48, v131
	v_cvt_pk_fp8_f32 v4, v5, v8
	v_mul_f32_e32 v8, 0x42800000, v21
	v_mul_f32_e32 v11, 0x42800000, v25
	v_mov_b32_e32 v5, v131
	v_cvt_pk_fp8_f32 v48, v49, v118
	v_mul_f32_e32 v74, 0x42800000, v87
	v_mul_f32_e32 v78, 0x42800000, v83
	v_mov_b32_e32 v49, v131
	v_cvt_pk_fp8_f32 v5, v8, v11
	v_cvt_pk_fp8_f32 v49, v74, v78
	v_mul_f32_e32 v9, 0x42800000, v13
	v_mul_f32_e32 v10, 0x42800000, v17
	v_mul_f32_e32 v74, 0x42800000, v95
	v_mul_f32_e32 v78, 0x42800000, v91
	v_cvt_pk_fp8_f32 v4, v9, v10 op_sel:[0,0,1]
	v_mul_f32_e32 v8, 0x42800000, v29
	v_mul_f32_e32 v9, 0x42800000, v33
	v_cvt_pk_fp8_f32 v48, v74, v78 op_sel:[0,0,1]
	v_mul_f32_e32 v74, 0x42800000, v75
	v_mul_f32_e32 v75, 0x42800000, v79
	v_cvt_pk_fp8_f32 v5, v8, v9 op_sel:[0,0,1]
	v_lshl_add_u64 v[188:189], v[120:121], 0, s[18:19]
	v_mul_f32_e32 v119, 0x42800000, v100
	v_mul_f32_e32 v120, 0x42800000, v104
	v_cvt_pk_fp8_f32 v49, v74, v75 op_sel:[0,0,1]
	v_mov_b32_e32 v74, v131
	ds_write_b64 v238, v[34:35]
	ds_write_b64 v238, v[2:3] offset:128
	ds_write_b64 v238, v[6:7] offset:256
	ds_write_b64 v238, v[4:5] offset:384
	v_lshl_add_u64 v[168:169], v[168:169], 0, s[18:19]
	v_lshl_add_u64 v[172:173], v[172:173], 0, s[18:19]
	v_lshl_add_u64 v[176:177], v[176:177], 0, s[18:19]
	v_lshl_add_u64 v[180:181], v[128:129], 0, s[18:19]
	v_lshl_add_u64 v[184:185], v[124:125], 0, s[18:19]
	v_lshl_add_u64 v[192:193], v[116:117], 0, s[18:19]
	v_cvt_pk_fp8_f32 v74, v119, v120
	v_mul_f32_e32 v86, 0x42800000, v88
	v_mul_f32_e32 v84, 0x42800000, v84
	v_mov_b32_e32 v75, v131
	v_lshl_add_u64 v[196:197], v[112:113], 0, s[18:19]
	v_lshl_add_u64 v[170:171], v[170:171], 0, s[18:19]
	global_load_dwordx4 v[2:5], v[168:169], off offset:256 nt
	global_load_dwordx4 v[6:9], v[170:171], off offset:256 nt
	v_lshl_add_u64 v[174:175], v[174:175], 0, s[18:19]
	global_load_dwordx4 v[10:13], v[172:173], off offset:256 nt
	global_load_dwordx4 v[14:17], v[174:175], off offset:256 nt
	v_lshl_add_u64 v[178:179], v[178:179], 0, s[18:19]
	global_load_dwordx4 v[18:21], v[176:177], off offset:256 nt
	global_load_dwordx4 v[22:25], v[178:179], off offset:256 nt
	v_lshl_add_u64 v[182:183], v[126:127], 0, s[18:19]
	global_load_dwordx4 v[26:29], v[180:181], off offset:256 nt
	global_load_dwordx4 v[30:33], v[182:183], off offset:256 nt
	v_lshl_add_u64 v[186:187], v[122:123], 0, s[18:19]
	global_load_dwordx4 v[34:37], v[184:185], off offset:256 nt
	global_load_dwordx4 v[38:41], v[186:187], off offset:256 nt
	v_mul_f32_e32 v121, 0x42800000, v101
	v_mul_f32_e32 v122, 0x42800000, v105
	global_load_dwordx4 v[98:101], v[188:189], off offset:256 nt
	global_load_dwordx4 v[102:105], v[190:191], off offset:256 nt
	v_lshl_add_u64 v[194:195], v[114:115], 0, s[18:19]
	v_mul_f32_e32 v79, 0x42800000, v92
	v_mul_f32_e32 v83, 0x42800000, v93
	v_cvt_pk_fp8_f32 v75, v86, v84
	v_mul_f32_e32 v84, 0x42800000, v89
	global_load_dwordx4 v[86:89], v[192:193], off offset:256 nt
	global_load_dwordx4 v[90:93], v[194:195], off offset:256 nt
	v_lshl_add_u64 v[198:199], v[110:111], 0, s[18:19]
	global_load_dwordx4 v[110:113], v[196:197], off offset:256 nt
	global_load_dwordx4 v[114:117], v[198:199], off offset:256 nt
	v_mul_f32_e32 v78, 0x42800000, v96
	v_cvt_pk_fp8_f32 v74, v78, v79 op_sel:[0,0,1]
	v_mul_f32_e32 v76, 0x42800000, v76
	v_mul_f32_e32 v78, 0x42800000, v80
	v_mul_f32_e32 v85, 0x42800000, v85
	v_cvt_pk_fp8_f32 v75, v76, v78 op_sel:[0,0,1]
	v_mov_b32_e32 v78, v131
	v_mov_b32_e32 v79, v131
	v_cvt_pk_fp8_f32 v78, v121, v122
	v_cvt_pk_fp8_f32 v79, v84, v85
	v_mul_f32_e32 v82, 0x42800000, v97
	v_mul_f32_e32 v76, 0x42800000, v77
	v_mul_f32_e32 v77, 0x42800000, v81
	v_cvt_pk_fp8_f32 v78, v82, v83 op_sel:[0,0,1]
	v_cvt_pk_fp8_f32 v79, v76, v77 op_sel:[0,0,1]
	ds_write_b64 v240, v[46:47]
	ds_write_b64 v240, v[48:49] offset:128
	ds_write_b64 v240, v[74:75] offset:256
	ds_write_b64 v240, v[78:79] offset:384
	s_waitcnt vmcnt(23)
	v_mul_f32_e32 v47, 0x42800000, v66
	s_waitcnt vmcnt(22)
	v_mul_f32_e32 v48, 0x42800000, v70
	v_mov_b32_e32 v46, v131
	v_cvt_pk_fp8_f32 v46, v47, v48
	s_waitcnt vmcnt(19)
	v_mul_f32_e32 v42, 0x42800000, v42
	s_waitcnt vmcnt(18)
	v_mul_f32_e32 v48, 0x42800000, v50
	v_mov_b32_e32 v47, v131
	v_cvt_pk_fp8_f32 v47, v42, v48
	v_mul_f32_e32 v49, 0x42800000, v58
	v_mul_f32_e32 v58, 0x42800000, v62
	s_waitcnt vmcnt(17)
	v_mul_f32_e32 v42, 0x42800000, v54
	s_waitcnt vmcnt(16)
	v_mul_f32_e32 v48, 0x42800000, v106
	v_cvt_pk_fp8_f32 v46, v49, v58 op_sel:[0,0,1]
	v_cvt_pk_fp8_f32 v47, v42, v48 op_sel:[0,0,1]
	v_mul_f32_e32 v48, 0x42800000, v67
	v_mul_f32_e32 v49, 0x42800000, v71
	v_mov_b32_e32 v42, v131
	v_cvt_pk_fp8_f32 v42, v48, v49
	v_mul_f32_e32 v48, 0x42800000, v43
	v_mul_f32_e32 v49, 0x42800000, v51
	v_mov_b32_e32 v43, v131
	v_cvt_pk_fp8_f32 v43, v48, v49
	v_mul_f32_e32 v50, 0x42800000, v59
	v_mul_f32_e32 v54, 0x42800000, v63
	v_mul_f32_e32 v48, 0x42800000, v55
	v_mul_f32_e32 v49, 0x42800000, v107
	v_cvt_pk_fp8_f32 v42, v50, v54 op_sel:[0,0,1]
	v_cvt_pk_fp8_f32 v43, v48, v49 op_sel:[0,0,1]
	v_mul_f32_e32 v49, 0x42800000, v68
	v_mul_f32_e32 v50, 0x42800000, v72
	v_mov_b32_e32 v48, v131
	v_cvt_pk_fp8_f32 v48, v49, v50
	v_mul_f32_e32 v44, 0x42800000, v44
	v_mul_f32_e32 v50, 0x42800000, v52
	v_mov_b32_e32 v49, v131
	v_cvt_pk_fp8_f32 v49, v44, v50
	v_mul_f32_e32 v51, 0x42800000, v60
	v_mul_f32_e32 v54, 0x42800000, v64
	v_mul_f32_e32 v44, 0x42800000, v56
	v_mul_f32_e32 v50, 0x42800000, v108
	v_cvt_pk_fp8_f32 v48, v51, v54 op_sel:[0,0,1]
	v_cvt_pk_fp8_f32 v49, v44, v50 op_sel:[0,0,1]
	v_mul_f32_e32 v50, 0x42800000, v69
	v_mul_f32_e32 v51, 0x42800000, v73
	v_mov_b32_e32 v44, v131
	v_cvt_pk_fp8_f32 v44, v50, v51
	v_mul_f32_e32 v50, 0x42800000, v45
	v_mul_f32_e32 v51, 0x42800000, v53
	v_mov_b32_e32 v45, v131
	v_cvt_pk_fp8_f32 v45, v50, v51
	v_mul_f32_e32 v52, 0x42800000, v61
	v_mul_f32_e32 v54, 0x42800000, v65
	v_mul_f32_e32 v50, 0x42800000, v57
	v_mul_f32_e32 v51, 0x42800000, v109
	v_cvt_pk_fp8_f32 v44, v52, v54 op_sel:[0,0,1]
	v_cvt_pk_fp8_f32 v45, v50, v51 op_sel:[0,0,1]
	ds_write_b64 v242, v[46:47]
	ds_write_b64 v242, v[42:43] offset:128
	ds_write_b64 v242, v[48:49] offset:256
	ds_write_b64 v242, v[44:45] offset:384
	ds_read_b128 v[42:45], v244
	v_cndmask_b32_e64 v46, v201, v200, s[6:7]
	v_or_b32_e32 v46, s8, v46
	v_mov_b32_e32 v47, v131
	v_lshlrev_b64 v[46:47], 11, v[46:47]
	v_lshl_add_u64 v[50:51], v[134:135], 0, v[46:47]
	ds_read_b128 v[46:49], v246
	s_waitcnt lgkmcnt(1)
	global_store_dwordx4 v[50:51], v[42:45], off nt
	s_waitcnt vmcnt(1)
	v_mul_f32_e32 v107, 0x42800000, v114
	v_mul_f32_e32 v108, 0x42800000, v110
	v_or_b32_e32 v42, 8, v200
	v_cndmask_b32_e64 v42, v202, v42, s[6:7]
	v_or_b32_e32 v42, s8, v42
	v_mov_b32_e32 v43, v131
	v_lshlrev_b64 v[42:43], 11, v[42:43]
	v_lshl_add_u64 v[42:43], v[134:135], 0, v[42:43]
	s_waitcnt lgkmcnt(0)
	global_store_dwordx4 v[42:43], v[46:49], off nt
	ds_read_b128 v[42:45], v248
	v_mov_b32_e32 v106, v131
	v_or_b32_e32 v46, 16, v200
	v_cndmask_b32_e64 v46, v210, v46, s[6:7]
	v_or_b32_e32 v46, s8, v46
	v_mov_b32_e32 v47, v131
	v_lshlrev_b64 v[46:47], 11, v[46:47]
	v_lshl_add_u64 v[50:51], v[134:135], 0, v[46:47]
	ds_read_b128 v[46:49], v250
	s_waitcnt lgkmcnt(1)
	global_store_dwordx4 v[50:51], v[42:45], off nt
	v_cvt_pk_fp8_f32 v106, v107, v108
	v_mul_f32_e32 v102, 0x42800000, v102
	v_cndmask_b32_e64 v42, v211, v203, s[6:7]
	v_or_b32_e32 v42, s8, v42
	v_mov_b32_e32 v43, v131
	v_lshlrev_b64 v[42:43], 11, v[42:43]
	v_lshl_add_u64 v[42:43], v[134:135], 0, v[42:43]
	s_waitcnt lgkmcnt(0)
	global_store_dwordx4 v[42:43], v[46:49], off nt
	ds_read_b128 v[42:45], v252
	v_mul_f32_e32 v98, 0x42800000, v98
	v_or_b32_e32 v46, 32, v200
	v_cndmask_b32_e64 v46, v212, v46, s[6:7]
	v_or_b32_e32 v46, s8, v46
	v_mov_b32_e32 v47, v131
	v_lshlrev_b64 v[46:47], 11, v[46:47]
	v_lshl_add_u64 v[50:51], v[134:135], 0, v[46:47]
	ds_read_b128 v[46:49], v204
	s_waitcnt lgkmcnt(1)
	global_store_dwordx4 v[50:51], v[42:45], off nt
	v_mov_b32_e32 v107, v131
	v_cvt_pk_fp8_f32 v107, v102, v98
	v_cndmask_b32_e64 v42, v213, v205, s[6:7]
	v_or_b32_e32 v42, s8, v42
	v_mov_b32_e32 v43, v131
	v_lshlrev_b64 v[42:43], 11, v[42:43]
	v_lshl_add_u64 v[42:43], v[134:135], 0, v[42:43]
	s_waitcnt lgkmcnt(0)
	global_store_dwordx4 v[42:43], v[46:49], off nt
	ds_read_b128 v[42:45], v216
	v_mul_f32_e32 v109, 0x42800000, v115
	v_cndmask_b32_e64 v46, v214, v228, s[6:7]
	v_or_b32_e32 v46, s8, v46
	v_mov_b32_e32 v47, v131
	v_lshlrev_b64 v[46:47], 11, v[46:47]
	v_lshl_add_u64 v[50:51], v[134:135], 0, v[46:47]
	ds_read_b128 v[46:49], v220
	s_waitcnt lgkmcnt(1)
	global_store_dwordx4 v[50:51], v[42:45], off nt
	v_mul_f32_e32 v110, 0x42800000, v111
	v_mul_f32_e32 v38, 0x42800000, v38
	v_cndmask_b32_e64 v42, v215, v232, s[6:7]
	v_or_b32_e32 v42, s8, v42
	v_mov_b32_e32 v43, v131
	v_lshlrev_b64 v[42:43], 11, v[42:43]
	v_lshl_add_u64 v[42:43], v[134:135], 0, v[42:43]
	s_waitcnt lgkmcnt(0)
	global_store_dwordx4 v[42:43], v[46:49], off nt
	global_load_dwordx4 v[74:77], v[136:137], off offset:256 nt
	global_load_dwordx4 v[78:81], v[138:139], off offset:256 nt
	global_load_dwordx4 v[94:97], v[140:141], off offset:256 nt
	global_load_dwordx4 v[82:85], v[142:143], off offset:256 nt
	global_load_dwordx4 v[70:73], v[144:145], off offset:256 nt
	global_load_dwordx4 v[66:69], v[146:147], off offset:256 nt
	global_load_dwordx4 v[58:61], v[148:149], off offset:256 nt
	global_load_dwordx4 v[62:65], v[150:151], off offset:256 nt
	global_load_dwordx4 v[42:45], v[152:153], off offset:256 nt
	global_load_dwordx4 v[46:49], v[154:155], off offset:256 nt
	v_mul_f32_e32 v34, 0x42800000, v34
	v_mov_b32_e32 v108, v131
	v_cvt_pk_fp8_f32 v107, v38, v34 op_sel:[0,0,1]
	v_cvt_pk_fp8_f32 v108, v109, v110
	v_mul_f32_e32 v34, 0x42800000, v103
	v_mul_f32_e32 v38, 0x42800000, v99
	v_mov_b32_e32 v109, v131
	v_cvt_pk_fp8_f32 v109, v34, v38
	v_mul_f32_e32 v34, 0x42800000, v91
	v_mul_f32_e32 v38, 0x42800000, v87
	v_cvt_pk_fp8_f32 v108, v34, v38 op_sel:[0,0,1]
	v_mul_f32_e32 v34, 0x42800000, v39
	v_mul_f32_e32 v35, 0x42800000, v35
	v_mul_f32_e32 v111, 0x42800000, v116
	v_mul_f32_e32 v112, 0x42800000, v112
	v_mul_f32_e32 v90, 0x42800000, v90
	v_mul_f32_e32 v86, 0x42800000, v86
	v_cvt_pk_fp8_f32 v109, v34, v35 op_sel:[0,0,1]
	v_mov_b32_e32 v34, v131
	v_cvt_pk_fp8_f32 v106, v90, v86 op_sel:[0,0,1]
	v_cvt_pk_fp8_f32 v34, v111, v112
	v_mul_f32_e32 v86, 0x42800000, v104
	v_mul_f32_e32 v87, 0x42800000, v100
	v_mov_b32_e32 v35, v131
	global_load_dwordx4 v[50:53], v[156:157], off offset:256 nt
	global_load_dwordx4 v[54:57], v[158:159], off offset:256 nt
	v_mul_f32_e32 v38, 0x42800000, v92
	v_mul_f32_e32 v110, 0x42800000, v93
	v_mul_f32_e32 v39, 0x42800000, v88
	v_mul_f32_e32 v115, 0x42800000, v89
	v_cvt_pk_fp8_f32 v35, v86, v87
	global_load_dwordx4 v[86:89], v[164:165], off offset:256 nt
	global_load_dwordx4 v[90:93], v[166:167], off offset:256 nt
	v_mul_f32_e32 v98, 0x42800000, v105
	v_mul_f32_e32 v99, 0x42800000, v101
	v_cvt_pk_fp8_f32 v34, v38, v39 op_sel:[0,0,1]
	v_mov_b32_e32 v39, v131
	v_cvt_pk_fp8_f32 v39, v98, v99
	global_load_dwordx4 v[98:101], v[160:161], off offset:256 nt
	global_load_dwordx4 v[102:105], v[162:163], off offset:256 nt
	v_mul_f32_e32 v38, 0x42800000, v40
	v_mul_f32_e32 v36, 0x42800000, v36
	v_mul_f32_e32 v114, 0x42800000, v117
	v_mul_f32_e32 v113, 0x42800000, v113
	v_cvt_pk_fp8_f32 v35, v38, v36 op_sel:[0,0,1]
	v_mov_b32_e32 v38, v131
	v_cvt_pk_fp8_f32 v38, v114, v113
	v_mul_f32_e32 v36, 0x42800000, v41
	v_mul_f32_e32 v37, 0x42800000, v37
	v_cvt_pk_fp8_f32 v39, v36, v37 op_sel:[0,0,1]
	v_cvt_pk_fp8_f32 v38, v110, v115 op_sel:[0,0,1]
	ds_write_b64 v236, v[106:107]
	ds_write_b64 v236, v[108:109] offset:128
	ds_write_b64 v236, v[34:35] offset:256
	ds_write_b64 v236, v[38:39] offset:384
	v_mul_f32_e32 v14, 0x42800000, v14
	v_mul_f32_e32 v10, 0x42800000, v10
	v_mov_b32_e32 v35, v131
	v_cvt_pk_fp8_f32 v35, v14, v10
	v_mul_f32_e32 v6, 0x42800000, v6
	v_mul_f32_e32 v2, 0x42800000, v2
	v_mov_b32_e32 v10, v131
	v_cvt_pk_fp8_f32 v35, v6, v2 op_sel:[0,0,1]
	v_mul_f32_e32 v2, 0x42800000, v31
	v_mul_f32_e32 v6, 0x42800000, v27
	v_cvt_pk_fp8_f32 v10, v2, v6
	v_mul_f32_e32 v2, 0x42800000, v15
	v_mul_f32_e32 v6, 0x42800000, v11
	v_mov_b32_e32 v11, v131
	v_cvt_pk_fp8_f32 v11, v2, v6
	v_mov_b32_e32 v106, v131
	v_mul_f32_e32 v30, 0x42800000, v30
	v_mul_f32_e32 v26, 0x42800000, v26
	v_mov_b32_e32 v34, v131
	v_mul_f32_e32 v2, 0x42800000, v7
	v_mul_f32_e32 v3, 0x42800000, v3
	s_waitcnt vmcnt(15)
	v_mul_f32_e32 v107, 0x42800000, v74
	s_waitcnt vmcnt(14)
	v_mul_f32_e32 v108, 0x42800000, v78
	v_cvt_pk_fp8_f32 v106, v107, v108
	v_mov_b32_e32 v107, v131
	s_waitcnt vmcnt(11)
	v_mul_f32_e32 v70, 0x42800000, v70
	s_waitcnt vmcnt(10)
	v_mul_f32_e32 v66, 0x42800000, v66
	v_cvt_pk_fp8_f32 v107, v70, v66
	v_cvt_pk_fp8_f32 v34, v30, v26
	v_cvt_pk_fp8_f32 v11, v2, v3 op_sel:[0,0,1]
	v_mul_f32_e32 v3, 0x42800000, v32
	v_mul_f32_e32 v6, 0x42800000, v28
	v_mov_b32_e32 v2, v131
	v_mul_f32_e32 v66, 0x42800000, v94
	v_mul_f32_e32 v70, 0x42800000, v82
	v_cvt_pk_fp8_f32 v2, v3, v6
	v_mul_f32_e32 v6, 0x42800000, v16
	v_mul_f32_e32 v12, 0x42800000, v12
	v_mov_b32_e32 v3, v131
	v_mul_f32_e32 v109, 0x42800000, v75
	v_mul_f32_e32 v110, 0x42800000, v79
	v_cvt_pk_fp8_f32 v106, v66, v70 op_sel:[0,0,1]
	s_waitcnt vmcnt(9)
	v_mul_f32_e32 v58, 0x42800000, v58
	s_waitcnt vmcnt(8)
	v_mul_f32_e32 v62, 0x42800000, v62
	v_mov_b32_e32 v66, v131
	v_cvt_pk_fp8_f32 v3, v6, v12
	v_cvt_pk_fp8_f32 v107, v58, v62 op_sel:[0,0,1]
	v_cvt_pk_fp8_f32 v66, v109, v110
	v_mul_f32_e32 v58, 0x42800000, v71
	v_mul_f32_e32 v62, 0x42800000, v67
	v_mov_b32_e32 v67, v131
	v_mul_f32_e32 v22, 0x42800000, v22
	v_mul_f32_e32 v18, 0x42800000, v18
	v_cvt_pk_fp8_f32 v67, v58, v62
	v_cvt_pk_fp8_f32 v34, v22, v18 op_sel:[0,0,1]
	v_mul_f32_e32 v14, 0x42800000, v23
	v_mul_f32_e32 v18, 0x42800000, v19
	v_cvt_pk_fp8_f32 v10, v14, v18 op_sel:[0,0,1]
	v_mul_f32_e32 v7, 0x42800000, v24
	v_mul_f32_e32 v14, 0x42800000, v20
	v_mul_f32_e32 v6, 0x42800000, v8
	v_mul_f32_e32 v4, 0x42800000, v4
	v_mul_f32_e32 v58, 0x42800000, v95
	v_mul_f32_e32 v62, 0x42800000, v83
	v_cvt_pk_fp8_f32 v2, v7, v14 op_sel:[0,0,1]
	v_cvt_pk_fp8_f32 v3, v6, v4 op_sel:[0,0,1]
	v_mul_f32_e32 v4, 0x42800000, v33
	v_mul_f32_e32 v7, 0x42800000, v29
	v_mov_b32_e32 v6, v131
	v_cvt_pk_fp8_f32 v66, v58, v62 op_sel:[0,0,1]
	v_mul_f32_e32 v58, 0x42800000, v59
	v_mul_f32_e32 v59, 0x42800000, v63
	v_cvt_pk_fp8_f32 v6, v4, v7
	v_mul_f32_e32 v4, 0x42800000, v17
	v_mul_f32_e32 v13, 0x42800000, v13
	v_mov_b32_e32 v7, v131
	v_mul_f32_e32 v111, 0x42800000, v76
	v_mul_f32_e32 v112, 0x42800000, v80
	v_cvt_pk_fp8_f32 v67, v58, v59 op_sel:[0,0,1]
	v_mov_b32_e32 v58, v131
	v_cvt_pk_fp8_f32 v7, v4, v13
	v_cvt_pk_fp8_f32 v58, v111, v112
	v_mul_f32_e32 v72, 0x42800000, v72
	v_mul_f32_e32 v68, 0x42800000, v68
	v_mov_b32_e32 v59, v131
	v_cvt_pk_fp8_f32 v59, v72, v68
	v_mul_f32_e32 v8, 0x42800000, v25
	v_mul_f32_e32 v12, 0x42800000, v21
	v_mul_f32_e32 v4, 0x42800000, v9
	v_mul_f32_e32 v5, 0x42800000, v5
	v_mul_f32_e32 v62, 0x42800000, v96
	v_mul_f32_e32 v63, 0x42800000, v84
	v_cvt_pk_fp8_f32 v6, v8, v12 op_sel:[0,0,1]
	v_cvt_pk_fp8_f32 v7, v4, v5 op_sel:[0,0,1]
	v_cvt_pk_fp8_f32 v58, v62, v63 op_sel:[0,0,1]
	v_mul_f32_e32 v60, 0x42800000, v60
	v_mul_f32_e32 v62, 0x42800000, v64
	ds_write_b64 v238, v[34:35]
	ds_write_b64 v238, v[10:11] offset:128
	ds_write_b64 v238, v[2:3] offset:256
	ds_write_b64 v238, v[6:7] offset:384
	v_mul_f32_e32 v113, 0x42800000, v77
	v_mul_f32_e32 v114, 0x42800000, v81
	v_mul_f32_e32 v68, 0x42800000, v73
	v_mul_f32_e32 v69, 0x42800000, v69
	v_cvt_pk_fp8_f32 v59, v60, v62 op_sel:[0,0,1]
	v_mov_b32_e32 v62, v131
	v_mov_b32_e32 v63, v131
	global_load_dwordx4 v[2:5], v[168:169], off offset:512 nt
	global_load_dwordx4 v[6:9], v[170:171], off offset:512 nt
	global_load_dwordx4 v[10:13], v[172:173], off offset:512 nt
	global_load_dwordx4 v[14:17], v[174:175], off offset:512 nt
	global_load_dwordx4 v[18:21], v[176:177], off offset:512 nt
	global_load_dwordx4 v[22:25], v[178:179], off offset:512 nt
	global_load_dwordx4 v[26:29], v[180:181], off offset:512 nt
	global_load_dwordx4 v[30:33], v[182:183], off offset:512 nt
	global_load_dwordx4 v[34:37], v[184:185], off offset:512 nt
	global_load_dwordx4 v[38:41], v[186:187], off offset:512 nt
	global_load_dwordx4 v[74:77], v[188:189], off offset:512 nt
	global_load_dwordx4 v[78:81], v[190:191], off offset:512 nt
	v_mul_f32_e32 v71, 0x42800000, v85
	global_load_dwordx4 v[122:125], v[192:193], off offset:512 nt
	global_load_dwordx4 v[126:129], v[194:195], off offset:512 nt
	v_cvt_pk_fp8_f32 v62, v113, v114
	v_cvt_pk_fp8_f32 v63, v68, v69
	global_load_dwordx4 v[82:85], v[196:197], off offset:512 nt
	global_load_dwordx4 v[206:209], v[198:199], off offset:512 nt
	v_mul_f32_e32 v70, 0x42800000, v97
	v_mul_f32_e32 v60, 0x42800000, v61
	v_mul_f32_e32 v61, 0x42800000, v65
	v_cvt_pk_fp8_f32 v62, v70, v71 op_sel:[0,0,1]
	v_cvt_pk_fp8_f32 v63, v60, v61 op_sel:[0,0,1]
	ds_write_b64 v240, v[106:107]
	ds_write_b64 v240, v[66:67] offset:128
	ds_write_b64 v240, v[58:59] offset:256
	ds_write_b64 v240, v[62:63] offset:384
	s_waitcnt vmcnt(23)
	v_mul_f32_e32 v42, 0x42800000, v42
	s_waitcnt vmcnt(22)
	v_mul_f32_e32 v46, 0x42800000, v46
	v_mov_b32_e32 v58, v131
	v_cvt_pk_fp8_f32 v58, v42, v46
	s_waitcnt vmcnt(19)
	v_mul_f32_e32 v42, 0x42800000, v86
	s_waitcnt vmcnt(18)
	v_mul_f32_e32 v46, 0x42800000, v90
	v_mov_b32_e32 v59, v131
	v_cvt_pk_fp8_f32 v59, v42, v46
	s_waitcnt vmcnt(17)
	v_mul_f32_e32 v42, 0x42800000, v98
	s_waitcnt vmcnt(16)
	v_mul_f32_e32 v46, 0x42800000, v102
	v_mul_f32_e32 v43, 0x42800000, v43
	v_cvt_pk_fp8_f32 v59, v42, v46 op_sel:[0,0,1]
	v_mul_f32_e32 v46, 0x42800000, v47
	v_mov_b32_e32 v42, v131
	v_mul_f32_e32 v47, 0x42800000, v51
	v_cvt_pk_fp8_f32 v42, v43, v46
	v_mul_f32_e32 v46, 0x42800000, v87
	v_mul_f32_e32 v51, 0x42800000, v91
	v_mov_b32_e32 v43, v131
	v_cvt_pk_fp8_f32 v43, v46, v51
	v_mul_f32_e32 v50, 0x42800000, v50
	v_mul_f32_e32 v54, 0x42800000, v54
	v_cvt_pk_fp8_f32 v58, v50, v54 op_sel:[0,0,1]
	v_mul_f32_e32 v50, 0x42800000, v55
	v_cvt_pk_fp8_f32 v42, v47, v50 op_sel:[0,0,1]
	v_mul_f32_e32 v46, 0x42800000, v99
	v_mul_f32_e32 v47, 0x42800000, v103
	v_cvt_pk_fp8_f32 v43, v46, v47 op_sel:[0,0,1]
	v_mul_f32_e32 v44, 0x42800000, v44
	v_mul_f32_e32 v47, 0x42800000, v48
	v_mov_b32_e32 v46, v131
	v_cvt_pk_fp8_f32 v46, v44, v47
	v_mul_f32_e32 v44, 0x42800000, v88
	v_mul_f32_e32 v51, 0x42800000, v92
	v_mov_b32_e32 v47, v131
	v_cvt_pk_fp8_f32 v47, v44, v51
	v_mul_f32_e32 v48, 0x42800000, v52
	v_mul_f32_e32 v50, 0x42800000, v56
	v_cvt_pk_fp8_f32 v46, v48, v50 op_sel:[0,0,1]
	v_mul_f32_e32 v44, 0x42800000, v100
	v_mul_f32_e32 v48, 0x42800000, v104
	v_cvt_pk_fp8_f32 v47, v44, v48 op_sel:[0,0,1]
	v_mul_f32_e32 v45, 0x42800000, v45
	v_mul_f32_e32 v48, 0x42800000, v49
	v_mov_b32_e32 v44, v131
	v_cvt_pk_fp8_f32 v44, v45, v48
	v_mul_f32_e32 v48, 0x42800000, v89
	v_mul_f32_e32 v51, 0x42800000, v93
	v_mov_b32_e32 v45, v131
	v_cvt_pk_fp8_f32 v45, v48, v51
	v_mul_f32_e32 v49, 0x42800000, v53
	v_mul_f32_e32 v50, 0x42800000, v57
	v_cvt_pk_fp8_f32 v44, v49, v50 op_sel:[0,0,1]
	v_mul_f32_e32 v48, 0x42800000, v101
	v_mul_f32_e32 v49, 0x42800000, v105
	v_cvt_pk_fp8_f32 v45, v48, v49 op_sel:[0,0,1]
	ds_write_b64 v242, v[58:59]
	ds_write_b64 v242, v[42:43] offset:128
	ds_write_b64 v242, v[46:47] offset:256
	ds_write_b64 v242, v[44:45] offset:384
	ds_read_b128 v[42:45], v244
	v_or_b32_e32 v46, 64, v200
	v_cndmask_b32_e64 v46, v217, v46, s[6:7]
	v_or_b32_e32 v46, s8, v46
	v_mov_b32_e32 v47, v131
	v_lshlrev_b64 v[46:47], 11, v[46:47]
	v_lshl_add_u64 v[50:51], v[134:135], 0, v[46:47]
	ds_read_b128 v[46:49], v246
	s_waitcnt lgkmcnt(1)
	global_store_dwordx4 v[50:51], v[42:45], off nt
	s_waitcnt vmcnt(8)
	v_mul_f32_e32 v34, 0x42800000, v34
	s_waitcnt vmcnt(7)
	v_mul_f32_e32 v38, 0x42800000, v38
	v_or_b32_e32 v42, 0x48, v200
	v_cndmask_b32_e64 v42, v219, v42, s[6:7]
	v_or_b32_e32 v42, s8, v42
	v_mov_b32_e32 v43, v131
	v_lshlrev_b64 v[42:43], 11, v[42:43]
	v_lshl_add_u64 v[42:43], v[134:135], 0, v[42:43]
	s_waitcnt lgkmcnt(0)
	global_store_dwordx4 v[42:43], v[46:49], off nt
	ds_read_b128 v[42:45], v248
	v_mul_f32_e32 v35, 0x42800000, v35
	v_or_b32_e32 v46, 0x50, v200
	v_cndmask_b32_e64 v46, v221, v46, s[6:7]
	v_or_b32_e32 v46, s8, v46
	v_mov_b32_e32 v47, v131
	v_lshlrev_b64 v[46:47], 11, v[46:47]
	v_lshl_add_u64 v[50:51], v[134:135], 0, v[46:47]
	ds_read_b128 v[46:49], v250
	s_waitcnt lgkmcnt(1)
	global_store_dwordx4 v[50:51], v[42:45], off nt
	v_mul_f32_e32 v36, 0x42800000, v36
	v_mul_f32_e32 v37, 0x42800000, v37
	v_or_b32_e32 v42, 0x58, v200
	v_cndmask_b32_e64 v42, v223, v42, s[6:7]
	v_or_b32_e32 v42, s8, v42
	v_mov_b32_e32 v43, v131
	v_lshlrev_b64 v[42:43], 11, v[42:43]
	v_lshl_add_u64 v[42:43], v[134:135], 0, v[42:43]
	s_waitcnt lgkmcnt(0)
	global_store_dwordx4 v[42:43], v[46:49], off nt
	ds_read_b128 v[42:45], v252
	v_mul_f32_e32 v14, 0x42800000, v14
	v_or_b32_e32 v46, 0x60, v200
	v_cndmask_b32_e64 v46, v225, v46, s[6:7]
	v_or_b32_e32 v46, s8, v46
	v_mov_b32_e32 v47, v131
	v_lshlrev_b64 v[46:47], 11, v[46:47]
	v_lshl_add_u64 v[50:51], v[134:135], 0, v[46:47]
	ds_read_b128 v[46:49], v204
	s_waitcnt lgkmcnt(1)
	global_store_dwordx4 v[50:51], v[42:45], off nt
	v_mul_f32_e32 v10, 0x42800000, v10
	v_mul_f32_e32 v6, 0x42800000, v6
	v_or_b32_e32 v42, 0x68, v200
	v_cndmask_b32_e64 v42, v227, v42, s[6:7]
	v_or_b32_e32 v42, s8, v42
	v_mov_b32_e32 v43, v131
	v_lshlrev_b64 v[42:43], 11, v[42:43]
	v_lshl_add_u64 v[42:43], v[134:135], 0, v[42:43]
	s_waitcnt lgkmcnt(0)
	global_store_dwordx4 v[42:43], v[46:49], off nt
	ds_read_b128 v[42:45], v216
	v_mul_f32_e32 v2, 0x42800000, v2
	v_or_b32_e32 v46, 0x70, v200
	v_cndmask_b32_e64 v46, v229, v46, s[6:7]
	v_or_b32_e32 v46, s8, v46
	v_mov_b32_e32 v47, v131
	v_lshlrev_b64 v[46:47], 11, v[46:47]
	v_lshl_add_u64 v[50:51], v[134:135], 0, v[46:47]
	ds_read_b128 v[46:49], v220
	s_waitcnt lgkmcnt(1)
	global_store_dwordx4 v[50:51], v[42:45], off nt
	s_waitcnt vmcnt(12)
	v_mul_f32_e32 v51, 0x42800000, v74
	s_waitcnt vmcnt(8)
	v_mul_f32_e32 v50, 0x42800000, v85
	v_or_b32_e32 v42, 0x78, v200
	v_cndmask_b32_e64 v42, v231, v42, s[6:7]
	v_or_b32_e32 v42, s8, v42
	v_mov_b32_e32 v43, v131
	v_lshlrev_b64 v[42:43], 11, v[42:43]
	v_lshl_add_u64 v[42:43], v[134:135], 0, v[42:43]
	s_waitcnt lgkmcnt(0)
	global_store_dwordx4 v[42:43], v[46:49], off nt
	global_load_dwordx4 v[106:109], v[136:137], off offset:512 nt
	global_load_dwordx4 v[110:113], v[138:139], off offset:512 nt
	global_load_dwordx4 v[114:117], v[140:141], off offset:512 nt
	global_load_dwordx4 v[118:121], v[142:143], off offset:512 nt
	global_load_dwordx4 v[98:101], v[144:145], off offset:512 nt
	global_load_dwordx4 v[102:105], v[146:147], off offset:512 nt
	global_load_dwordx4 v[90:93], v[148:149], off offset:512 nt
	global_load_dwordx4 v[94:97], v[150:151], off offset:512 nt
	global_load_dwordx4 v[66:69], v[152:153], off offset:512 nt
	global_load_dwordx4 v[70:73], v[154:155], off offset:512 nt
	s_waitcnt vmcnt(18)
	v_mul_f32_e32 v43, 0x42800000, v206
	v_mul_f32_e32 v44, 0x42800000, v82
	v_mov_b32_e32 v42, v131
	v_cvt_pk_fp8_f32 v42, v43, v44
	v_mul_f32_e32 v44, 0x42800000, v78
	v_mov_b32_e32 v43, v131
	v_cvt_pk_fp8_f32 v43, v44, v51
	v_mul_f32_e32 v44, 0x42800000, v126
	v_mul_f32_e32 v51, 0x42800000, v122
	v_mul_f32_e32 v45, 0x42800000, v207
	v_mul_f32_e32 v46, 0x42800000, v83
	v_cvt_pk_fp8_f32 v42, v44, v51 op_sel:[0,0,1]
	v_mov_b32_e32 v44, v131
	v_cvt_pk_fp8_f32 v43, v38, v34 op_sel:[0,0,1]
	v_cvt_pk_fp8_f32 v44, v45, v46
	v_mul_f32_e32 v34, 0x42800000, v79
	v_mul_f32_e32 v38, 0x42800000, v75
	v_mov_b32_e32 v45, v131
	v_cvt_pk_fp8_f32 v45, v34, v38
	v_mul_f32_e32 v34, 0x42800000, v127
	v_mul_f32_e32 v38, 0x42800000, v123
	v_cvt_pk_fp8_f32 v44, v34, v38 op_sel:[0,0,1]
	v_mul_f32_e32 v34, 0x42800000, v39
	v_mul_f32_e32 v47, 0x42800000, v208
	v_mul_f32_e32 v48, 0x42800000, v84
	v_cvt_pk_fp8_f32 v45, v34, v35 op_sel:[0,0,1]
	v_mov_b32_e32 v34, v131
	v_cvt_pk_fp8_f32 v34, v47, v48
	v_mul_f32_e32 v47, 0x42800000, v80
	v_mul_f32_e32 v48, 0x42800000, v76
	v_mov_b32_e32 v35, v131
	global_load_dwordx4 v[82:85], v[156:157], off offset:512 nt
	global_load_dwordx4 v[86:89], v[158:159], off offset:512 nt
	v_mul_f32_e32 v39, 0x42800000, v124
	v_mul_f32_e32 v51, 0x42800000, v125
	v_cvt_pk_fp8_f32 v35, v47, v48
	v_mul_f32_e32 v47, 0x42800000, v81
	global_load_dwordx4 v[78:81], v[164:165], off offset:512 nt
	global_load_dwordx4 v[122:125], v[166:167], off offset:512 nt
	v_mul_f32_e32 v38, 0x42800000, v128
	v_mul_f32_e32 v46, 0x42800000, v129
	v_mul_f32_e32 v48, 0x42800000, v77
	global_load_dwordx4 v[74:77], v[160:161], off offset:512 nt
	global_load_dwordx4 v[126:129], v[162:163], off offset:512 nt
	v_cvt_pk_fp8_f32 v34, v38, v39 op_sel:[0,0,1]
	v_mul_f32_e32 v38, 0x42800000, v40
	v_mul_f32_e32 v49, 0x42800000, v209
	v_cvt_pk_fp8_f32 v35, v38, v36 op_sel:[0,0,1]
	v_mov_b32_e32 v38, v131
	v_mov_b32_e32 v39, v131
	v_cvt_pk_fp8_f32 v38, v49, v50
	v_cvt_pk_fp8_f32 v39, v47, v48
	v_mul_f32_e32 v36, 0x42800000, v41
	v_mul_f32_e32 v30, 0x42800000, v30
	v_cvt_pk_fp8_f32 v38, v46, v51 op_sel:[0,0,1]
	v_cvt_pk_fp8_f32 v39, v36, v37 op_sel:[0,0,1]
	ds_write_b64 v236, v[42:43]
	ds_write_b64 v236, v[44:45] offset:128
	ds_write_b64 v236, v[34:35] offset:256
	ds_write_b64 v236, v[38:39] offset:384
	v_mov_b32_e32 v35, v131
	v_cvt_pk_fp8_f32 v35, v14, v10
	v_mov_b32_e32 v10, v131
	v_mul_f32_e32 v26, 0x42800000, v26
	v_mov_b32_e32 v34, v131
	v_cvt_pk_fp8_f32 v35, v6, v2 op_sel:[0,0,1]
	v_mul_f32_e32 v2, 0x42800000, v31
	v_mul_f32_e32 v6, 0x42800000, v27
	v_cvt_pk_fp8_f32 v10, v2, v6
	v_mul_f32_e32 v2, 0x42800000, v15
	v_mul_f32_e32 v6, 0x42800000, v11
	v_mov_b32_e32 v11, v131
	v_cvt_pk_fp8_f32 v11, v2, v6
	v_mul_f32_e32 v2, 0x42800000, v7
	v_mul_f32_e32 v3, 0x42800000, v3
	v_cvt_pk_fp8_f32 v34, v30, v26
	v_cvt_pk_fp8_f32 v11, v2, v3 op_sel:[0,0,1]
	v_mul_f32_e32 v3, 0x42800000, v32
	v_mul_f32_e32 v6, 0x42800000, v28
	v_mov_b32_e32 v2, v131
	v_cvt_pk_fp8_f32 v2, v3, v6
	v_mul_f32_e32 v6, 0x42800000, v16
	v_mul_f32_e32 v12, 0x42800000, v12
	v_mov_b32_e32 v3, v131
	v_cvt_pk_fp8_f32 v3, v6, v12
	v_mul_f32_e32 v22, 0x42800000, v22
	v_mul_f32_e32 v18, 0x42800000, v18
	v_cvt_pk_fp8_f32 v34, v22, v18 op_sel:[0,0,1]
	v_mul_f32_e32 v14, 0x42800000, v23
	v_mul_f32_e32 v18, 0x42800000, v19
	v_cvt_pk_fp8_f32 v10, v14, v18 op_sel:[0,0,1]
	v_mul_f32_e32 v7, 0x42800000, v24
	v_mul_f32_e32 v14, 0x42800000, v20
	v_mul_f32_e32 v6, 0x42800000, v8
	v_mul_f32_e32 v4, 0x42800000, v4
	v_cvt_pk_fp8_f32 v2, v7, v14 op_sel:[0,0,1]
	v_cvt_pk_fp8_f32 v3, v6, v4 op_sel:[0,0,1]
	v_mul_f32_e32 v4, 0x42800000, v33
	v_mul_f32_e32 v7, 0x42800000, v29
	v_mov_b32_e32 v6, v131
	v_cvt_pk_fp8_f32 v6, v4, v7
	v_mul_f32_e32 v4, 0x42800000, v17
	v_mul_f32_e32 v13, 0x42800000, v13
	v_mov_b32_e32 v7, v131
	v_cvt_pk_fp8_f32 v7, v4, v13
	v_mul_f32_e32 v8, 0x42800000, v25
	v_mul_f32_e32 v12, 0x42800000, v21
	v_mul_f32_e32 v4, 0x42800000, v9
	v_mul_f32_e32 v5, 0x42800000, v5
	v_cvt_pk_fp8_f32 v6, v8, v12 op_sel:[0,0,1]
	v_cvt_pk_fp8_f32 v7, v4, v5 op_sel:[0,0,1]
	ds_write_b64 v238, v[34:35]
	ds_write_b64 v238, v[10:11] offset:128
	ds_write_b64 v238, v[2:3] offset:256
	ds_write_b64 v238, v[6:7] offset:384
	global_load_dwordx4 v[58:61], v[198:199], off offset:768 nt
	global_load_dwordx4 v[62:65], v[196:197], off offset:768 nt
	global_load_dwordx4 v[50:53], v[194:195], off offset:768 nt
	global_load_dwordx4 v[42:45], v[192:193], off offset:768 nt
	global_load_dwordx4 v[54:57], v[190:191], off offset:768 nt
	global_load_dwordx4 v[34:37], v[188:189], off offset:768 nt
	global_load_dwordx4 v[38:41], v[186:187], off offset:768 nt
	global_load_dwordx4 v[46:49], v[184:185], off offset:768 nt
	global_load_dwordx4 v[2:5], v[182:183], off offset:768 nt
	global_load_dwordx4 v[6:9], v[180:181], off offset:768 nt
	global_load_dwordx4 v[10:13], v[178:179], off offset:768 nt
	global_load_dwordx4 v[14:17], v[176:177], off offset:768 nt
	global_load_dwordx4 v[18:21], v[174:175], off offset:768 nt
	global_load_dwordx4 v[22:25], v[172:173], off offset:768 nt
	global_load_dwordx4 v[26:29], v[170:171], off offset:768 nt
	global_load_dwordx4 v[30:33], v[168:169], off offset:768 nt
	s_waitcnt vmcnt(27)
	v_mul_f32_e32 v98, 0x42800000, v98
	s_waitcnt vmcnt(26)
	v_mul_f32_e32 v102, 0x42800000, v102
	v_mov_b32_e32 v169, v131
	v_cvt_pk_fp8_f32 v169, v98, v102
	s_waitcnt vmcnt(25)
	v_mul_f32_e32 v90, 0x42800000, v90
	s_waitcnt vmcnt(24)
	v_mul_f32_e32 v94, 0x42800000, v94
	v_mov_b32_e32 v98, v131
	v_cvt_pk_fp8_f32 v169, v90, v94 op_sel:[0,0,1]
	v_mul_f32_e32 v90, 0x42800000, v107
	v_mul_f32_e32 v94, 0x42800000, v111
	v_cvt_pk_fp8_f32 v98, v90, v94
	v_mul_f32_e32 v90, 0x42800000, v99
	v_mul_f32_e32 v94, 0x42800000, v103
	v_mov_b32_e32 v99, v131
	v_cvt_pk_fp8_f32 v99, v90, v94
	v_mul_f32_e32 v90, 0x42800000, v91
	v_mul_f32_e32 v91, 0x42800000, v95
	v_mul_f32_e32 v94, 0x42800000, v112
	v_cvt_pk_fp8_f32 v99, v90, v91 op_sel:[0,0,1]
	v_mul_f32_e32 v91, 0x42800000, v108
	v_mov_b32_e32 v90, v131
	v_cvt_pk_fp8_f32 v90, v91, v94
	v_mul_f32_e32 v94, 0x42800000, v100
	v_mul_f32_e32 v100, 0x42800000, v104
	v_mov_b32_e32 v91, v131
	v_cvt_pk_fp8_f32 v91, v94, v100
	v_mul_f32_e32 v106, 0x42800000, v106
	v_mul_f32_e32 v110, 0x42800000, v110
	v_mov_b32_e32 v168, v131
	v_cvt_pk_fp8_f32 v168, v106, v110
	v_mul_f32_e32 v102, 0x42800000, v115
	v_mul_f32_e32 v106, 0x42800000, v119
	v_cvt_pk_fp8_f32 v98, v102, v106 op_sel:[0,0,1]
	v_mul_f32_e32 v95, 0x42800000, v116
	v_mul_f32_e32 v102, 0x42800000, v120
	v_mul_f32_e32 v92, 0x42800000, v92
	v_mul_f32_e32 v94, 0x42800000, v96
	v_cvt_pk_fp8_f32 v90, v95, v102 op_sel:[0,0,1]
	v_cvt_pk_fp8_f32 v91, v92, v94 op_sel:[0,0,1]
	v_mul_f32_e32 v92, 0x42800000, v109
	v_mul_f32_e32 v95, 0x42800000, v113
	v_mov_b32_e32 v94, v131
	v_cvt_pk_fp8_f32 v94, v92, v95
	v_mul_f32_e32 v92, 0x42800000, v101
	v_mul_f32_e32 v101, 0x42800000, v105
	v_mov_b32_e32 v95, v131
	v_mul_f32_e32 v114, 0x42800000, v114
	v_mul_f32_e32 v118, 0x42800000, v118
	v_cvt_pk_fp8_f32 v95, v92, v101
	v_cvt_pk_fp8_f32 v168, v114, v118 op_sel:[0,0,1]
	v_mul_f32_e32 v96, 0x42800000, v117
	v_mul_f32_e32 v100, 0x42800000, v121
	v_mul_f32_e32 v92, 0x42800000, v93
	v_mul_f32_e32 v93, 0x42800000, v97
	v_cvt_pk_fp8_f32 v94, v96, v100 op_sel:[0,0,1]
	v_cvt_pk_fp8_f32 v95, v92, v93 op_sel:[0,0,1]
	ds_write_b64 v240, v[168:169]
	ds_write_b64 v240, v[98:99] offset:128
	ds_write_b64 v240, v[90:91] offset:256
	ds_write_b64 v240, v[94:95] offset:384
	s_waitcnt vmcnt(23)
	v_mul_f32_e32 v66, 0x42800000, v66
	s_waitcnt vmcnt(22)
	v_mul_f32_e32 v70, 0x42800000, v70
	v_mov_b32_e32 v90, v131
	v_cvt_pk_fp8_f32 v90, v66, v70
	s_waitcnt vmcnt(19)
	v_mul_f32_e32 v66, 0x42800000, v78
	s_waitcnt vmcnt(18)
	v_mul_f32_e32 v70, 0x42800000, v122
	v_mov_b32_e32 v91, v131
	v_cvt_pk_fp8_f32 v91, v66, v70
	s_waitcnt vmcnt(17)
	v_mul_f32_e32 v66, 0x42800000, v74
	s_waitcnt vmcnt(16)
	v_mul_f32_e32 v70, 0x42800000, v126
	v_mul_f32_e32 v67, 0x42800000, v67
	v_cvt_pk_fp8_f32 v91, v66, v70 op_sel:[0,0,1]
	v_mul_f32_e32 v70, 0x42800000, v71
	v_mov_b32_e32 v66, v131
	v_cvt_pk_fp8_f32 v66, v67, v70
	v_mul_f32_e32 v70, 0x42800000, v79
	v_mul_f32_e32 v78, 0x42800000, v123
	v_mov_b32_e32 v67, v131
	v_cvt_pk_fp8_f32 v67, v70, v78
	v_mul_f32_e32 v71, 0x42800000, v83
	v_mul_f32_e32 v74, 0x42800000, v87
	v_cvt_pk_fp8_f32 v66, v71, v74 op_sel:[0,0,1]
	v_mul_f32_e32 v70, 0x42800000, v75
	v_mul_f32_e32 v71, 0x42800000, v127
	v_cvt_pk_fp8_f32 v67, v70, v71 op_sel:[0,0,1]
	v_mul_f32_e32 v68, 0x42800000, v68
	v_mul_f32_e32 v71, 0x42800000, v72
	v_mov_b32_e32 v70, v131
	v_cvt_pk_fp8_f32 v70, v68, v71
	v_mul_f32_e32 v68, 0x42800000, v80
	v_mul_f32_e32 v75, 0x42800000, v124
	v_mov_b32_e32 v71, v131
	v_cvt_pk_fp8_f32 v71, v68, v75
	v_mul_f32_e32 v72, 0x42800000, v84
	v_mul_f32_e32 v74, 0x42800000, v88
	v_cvt_pk_fp8_f32 v70, v72, v74 op_sel:[0,0,1]
	v_mul_f32_e32 v68, 0x42800000, v76
	v_mul_f32_e32 v72, 0x42800000, v128
	v_cvt_pk_fp8_f32 v71, v68, v72 op_sel:[0,0,1]
	v_mul_f32_e32 v69, 0x42800000, v69
	v_mul_f32_e32 v72, 0x42800000, v73
	v_mov_b32_e32 v68, v131
	v_cvt_pk_fp8_f32 v68, v69, v72
	v_mul_f32_e32 v72, 0x42800000, v81
	v_mul_f32_e32 v75, 0x42800000, v125
	v_mov_b32_e32 v69, v131
	v_mul_f32_e32 v82, 0x42800000, v82
	v_mul_f32_e32 v86, 0x42800000, v86
	v_cvt_pk_fp8_f32 v69, v72, v75
	v_cvt_pk_fp8_f32 v90, v82, v86 op_sel:[0,0,1]
	v_mul_f32_e32 v73, 0x42800000, v85
	v_mul_f32_e32 v74, 0x42800000, v89
	v_cvt_pk_fp8_f32 v68, v73, v74 op_sel:[0,0,1]
	v_mul_f32_e32 v72, 0x42800000, v77
	v_mul_f32_e32 v73, 0x42800000, v129
	v_cvt_pk_fp8_f32 v69, v72, v73 op_sel:[0,0,1]
	ds_write_b64 v242, v[90:91]
	ds_write_b64 v242, v[66:67] offset:128
	ds_write_b64 v242, v[70:71] offset:256
	ds_write_b64 v242, v[68:69] offset:384
	ds_read_b128 v[66:69], v244
	v_or_b32_e32 v70, 0x80, v200
	v_cndmask_b32_e64 v70, v233, v70, s[6:7]
	v_or_b32_e32 v70, s8, v70
	v_mov_b32_e32 v71, v131
	v_lshlrev_b64 v[70:71], 11, v[70:71]
	v_lshl_add_u64 v[74:75], v[134:135], 0, v[70:71]
	ds_read_b128 v[70:73], v246
	s_waitcnt lgkmcnt(1)
	global_store_dwordx4 v[74:75], v[66:69], off nt
	s_waitcnt vmcnt(16)
	v_mul_f32_e32 v90, 0x42800000, v58
	s_waitcnt vmcnt(15)
	v_mul_f32_e32 v91, 0x42800000, v62
	v_or_b32_e32 v66, 0x88, v200
	v_cndmask_b32_e64 v66, v235, v66, s[6:7]
	v_or_b32_e32 v66, s8, v66
	v_mov_b32_e32 v67, v131
	v_lshlrev_b64 v[66:67], 11, v[66:67]
	v_lshl_add_u64 v[66:67], v[134:135], 0, v[66:67]
	s_waitcnt lgkmcnt(0)
	global_store_dwordx4 v[66:67], v[70:73], off nt
	ds_read_b128 v[66:69], v248
	s_waitcnt vmcnt(15)
	v_mul_f32_e32 v92, 0x42800000, v50
	v_or_b32_e32 v70, 0x90, v200
	v_cndmask_b32_e64 v70, v237, v70, s[6:7]
	v_or_b32_e32 v70, s8, v70
	v_mov_b32_e32 v71, v131
	v_lshlrev_b64 v[70:71], 11, v[70:71]
	v_lshl_add_u64 v[74:75], v[134:135], 0, v[70:71]
	ds_read_b128 v[70:73], v250
	s_waitcnt lgkmcnt(1)
	global_store_dwordx4 v[74:75], v[66:69], off nt
	s_waitcnt vmcnt(15)
	v_mul_f32_e32 v93, 0x42800000, v42
	s_andn2_b64 vcc, exec, s[16:17]
	v_or_b32_e32 v66, 0x98, v200
	v_cndmask_b32_e64 v66, v239, v66, s[6:7]
	v_or_b32_e32 v66, s8, v66
	v_mov_b32_e32 v67, v131
	v_lshlrev_b64 v[66:67], 11, v[66:67]
	v_lshl_add_u64 v[66:67], v[134:135], 0, v[66:67]
	s_waitcnt lgkmcnt(0)
	global_store_dwordx4 v[66:67], v[70:73], off nt
	ds_read_b128 v[66:69], v252
	s_nop 0
	v_or_b32_e32 v70, 0xa0, v200
	v_cndmask_b32_e64 v70, v241, v70, s[6:7]
	v_or_b32_e32 v70, s8, v70
	v_mov_b32_e32 v71, v131
	v_lshlrev_b64 v[70:71], 11, v[70:71]
	v_lshl_add_u64 v[74:75], v[134:135], 0, v[70:71]
	ds_read_b128 v[70:73], v204
	s_waitcnt lgkmcnt(1)
	global_store_dwordx4 v[74:75], v[66:69], off nt
	s_nop 1
	v_or_b32_e32 v66, 0xa8, v200
	v_cndmask_b32_e64 v66, v243, v66, s[6:7]
	v_or_b32_e32 v66, s8, v66
	v_mov_b32_e32 v67, v131
	v_lshlrev_b64 v[66:67], 11, v[66:67]
	v_lshl_add_u64 v[66:67], v[134:135], 0, v[66:67]
	s_waitcnt lgkmcnt(0)
	global_store_dwordx4 v[66:67], v[70:73], off nt
	ds_read_b128 v[66:69], v216
	s_nop 0
	v_or_b32_e32 v70, 0xb0, v200
	v_cndmask_b32_e64 v70, v245, v70, s[6:7]
	v_or_b32_e32 v70, s8, v70
	v_mov_b32_e32 v71, v131
	v_lshlrev_b64 v[70:71], 11, v[70:71]
	v_lshl_add_u64 v[74:75], v[134:135], 0, v[70:71]
	ds_read_b128 v[70:73], v220
	s_waitcnt lgkmcnt(1)
	global_store_dwordx4 v[74:75], v[66:69], off nt
	s_nop 1
	v_or_b32_e32 v66, 0xb8, v200
	v_cndmask_b32_e64 v66, v247, v66, s[6:7]
	v_or_b32_e32 v66, s8, v66
	v_mov_b32_e32 v67, v131
	v_lshlrev_b64 v[66:67], 11, v[66:67]
	v_lshl_add_u64 v[66:67], v[134:135], 0, v[66:67]
	s_waitcnt lgkmcnt(0)
	global_store_dwordx4 v[66:67], v[70:73], off nt
	global_load_dwordx4 v[114:117], v[136:137], off offset:768 nt
	global_load_dwordx4 v[118:121], v[138:139], off offset:768 nt
	global_load_dwordx4 v[122:125], v[140:141], off offset:768 nt
	global_load_dwordx4 v[126:129], v[142:143], off offset:768 nt
	global_load_dwordx4 v[106:109], v[144:145], off offset:768 nt
	global_load_dwordx4 v[110:113], v[146:147], off offset:768 nt
	global_load_dwordx4 v[98:101], v[148:149], off offset:768 nt
	global_load_dwordx4 v[102:105], v[150:151], off offset:768 nt
	global_load_dwordx4 v[74:77], v[152:153], off offset:768 nt
	global_load_dwordx4 v[78:81], v[154:155], off offset:768 nt
	global_load_dwordx4 v[82:85], v[156:157], off offset:768 nt
	global_load_dwordx4 v[86:89], v[158:159], off offset:768 nt
	global_load_dwordx4 v[66:69], v[164:165], off offset:768 nt
	global_load_dwordx4 v[70:73], v[166:167], off offset:768 nt
	v_mov_b32_e32 v136, v131
	v_cvt_pk_fp8_f32 v136, v90, v91
	s_waitcnt vmcnt(33)
	v_mul_f32_e32 v90, 0x42800000, v54
	s_waitcnt vmcnt(32)
	v_mul_f32_e32 v91, 0x42800000, v34
	v_mov_b32_e32 v137, v131
	v_cvt_pk_fp8_f32 v137, v90, v91
	s_waitcnt vmcnt(31)
	v_mul_f32_e32 v90, 0x42800000, v38
	s_waitcnt vmcnt(30)
	v_mul_f32_e32 v91, 0x42800000, v46
	v_mov_b32_e32 v138, v131
	v_cvt_pk_fp8_f32 v137, v90, v91 op_sel:[0,0,1]
	v_mul_f32_e32 v90, 0x42800000, v59
	v_mul_f32_e32 v91, 0x42800000, v63
	v_cvt_pk_fp8_f32 v138, v90, v91
	v_mul_f32_e32 v90, 0x42800000, v55
	v_mul_f32_e32 v91, 0x42800000, v35
	v_mov_b32_e32 v139, v131
	v_cvt_pk_fp8_f32 v139, v90, v91
	v_mul_f32_e32 v90, 0x42800000, v39
	v_mul_f32_e32 v91, 0x42800000, v47
	v_mov_b32_e32 v140, v131
	v_cvt_pk_fp8_f32 v139, v90, v91 op_sel:[0,0,1]
	v_mul_f32_e32 v90, 0x42800000, v60
	v_mul_f32_e32 v91, 0x42800000, v64
	v_cvt_pk_fp8_f32 v140, v90, v91
	v_mul_f32_e32 v90, 0x42800000, v56
	v_mul_f32_e32 v91, 0x42800000, v36
	v_mov_b32_e32 v141, v131
	v_cvt_pk_fp8_f32 v141, v90, v91
	v_cvt_pk_fp8_f32 v136, v92, v93 op_sel:[0,0,1]
	v_mul_f32_e32 v92, 0x42800000, v51
	v_mul_f32_e32 v93, 0x42800000, v43
	v_cvt_pk_fp8_f32 v138, v92, v93 op_sel:[0,0,1]
	v_mul_f32_e32 v92, 0x42800000, v52
	v_mul_f32_e32 v93, 0x42800000, v44
	v_mul_f32_e32 v90, 0x42800000, v40
	v_mul_f32_e32 v91, 0x42800000, v48
	v_cvt_pk_fp8_f32 v140, v92, v93 op_sel:[0,0,1]
	v_cvt_pk_fp8_f32 v141, v90, v91 op_sel:[0,0,1]
	global_load_dwordx4 v[90:93], v[160:161], off offset:768 nt
	global_load_dwordx4 v[94:97], v[162:163], off offset:768 nt
	ds_write_b64 v236, v[136:137]
	ds_write_b64 v236, v[138:139] offset:128
	ds_write_b64 v236, v[140:141] offset:256
	v_mul_f32_e32 v137, 0x42800000, v61
	v_mul_f32_e32 v138, 0x42800000, v65
	v_mov_b32_e32 v136, v131
	v_cvt_pk_fp8_f32 v136, v137, v138
	v_mul_f32_e32 v138, 0x42800000, v57
	v_mul_f32_e32 v141, 0x42800000, v37
	v_mov_b32_e32 v137, v131
	v_cvt_pk_fp8_f32 v137, v138, v141
	v_mul_f32_e32 v139, 0x42800000, v53
	v_mul_f32_e32 v140, 0x42800000, v45
	v_cvt_pk_fp8_f32 v136, v139, v140 op_sel:[0,0,1]
	v_mul_f32_e32 v138, 0x42800000, v41
	v_mul_f32_e32 v139, 0x42800000, v49
	v_cvt_pk_fp8_f32 v137, v138, v139 op_sel:[0,0,1]
	s_waitcnt vmcnt(31)
	v_mul_f32_e32 v139, 0x42800000, v2
	s_waitcnt vmcnt(30)
	v_mul_f32_e32 v140, 0x42800000, v6
	v_mov_b32_e32 v138, v131
	v_cvt_pk_fp8_f32 v138, v139, v140
	s_waitcnt vmcnt(27)
	v_mul_f32_e32 v140, 0x42800000, v18
	s_waitcnt vmcnt(26)
	v_mul_f32_e32 v143, 0x42800000, v22
	v_mov_b32_e32 v139, v131
	v_cvt_pk_fp8_f32 v139, v140, v143
	v_mul_f32_e32 v141, 0x42800000, v10
	v_mul_f32_e32 v142, 0x42800000, v14
	v_cvt_pk_fp8_f32 v138, v141, v142 op_sel:[0,0,1]
	s_waitcnt vmcnt(25)
	v_mul_f32_e32 v140, 0x42800000, v26
	s_waitcnt vmcnt(24)
	v_mul_f32_e32 v141, 0x42800000, v30
	v_cvt_pk_fp8_f32 v139, v140, v141 op_sel:[0,0,1]
	v_mul_f32_e32 v141, 0x42800000, v3
	v_mul_f32_e32 v142, 0x42800000, v7
	v_mov_b32_e32 v140, v131
	v_cvt_pk_fp8_f32 v140, v141, v142
	v_mul_f32_e32 v142, 0x42800000, v19
	v_mul_f32_e32 v145, 0x42800000, v23
	v_mov_b32_e32 v141, v131
	v_cvt_pk_fp8_f32 v141, v142, v145
	v_mul_f32_e32 v143, 0x42800000, v11
	v_mul_f32_e32 v144, 0x42800000, v15
	v_cvt_pk_fp8_f32 v140, v143, v144 op_sel:[0,0,1]
	v_mul_f32_e32 v142, 0x42800000, v27
	v_mul_f32_e32 v143, 0x42800000, v31
	v_cvt_pk_fp8_f32 v141, v142, v143 op_sel:[0,0,1]
	v_mul_f32_e32 v143, 0x42800000, v4
	v_mul_f32_e32 v144, 0x42800000, v8
	v_mov_b32_e32 v142, v131
	v_cvt_pk_fp8_f32 v142, v143, v144
	v_mul_f32_e32 v144, 0x42800000, v20
	v_mul_f32_e32 v147, 0x42800000, v24
	v_mov_b32_e32 v143, v131
	v_cvt_pk_fp8_f32 v143, v144, v147
	v_mul_f32_e32 v145, 0x42800000, v12
	v_mul_f32_e32 v146, 0x42800000, v16
	v_cvt_pk_fp8_f32 v142, v145, v146 op_sel:[0,0,1]
	v_mul_f32_e32 v144, 0x42800000, v28
	v_mul_f32_e32 v145, 0x42800000, v32
	v_cvt_pk_fp8_f32 v143, v144, v145 op_sel:[0,0,1]
	ds_write_b64 v236, v[136:137] offset:384
	ds_write_b64 v238, v[138:139]
	ds_write_b64 v238, v[140:141] offset:128
	ds_write_b64 v238, v[142:143] offset:256
	v_mul_f32_e32 v137, 0x42800000, v5
	v_mul_f32_e32 v138, 0x42800000, v9
	v_mov_b32_e32 v136, v131
	v_cvt_pk_fp8_f32 v136, v137, v138
	v_mul_f32_e32 v138, 0x42800000, v21
	v_mul_f32_e32 v141, 0x42800000, v25
	v_mov_b32_e32 v137, v131
	v_cvt_pk_fp8_f32 v137, v138, v141
	v_mul_f32_e32 v139, 0x42800000, v13
	v_mul_f32_e32 v140, 0x42800000, v17
	v_cvt_pk_fp8_f32 v136, v139, v140 op_sel:[0,0,1]
	v_mul_f32_e32 v138, 0x42800000, v29
	v_mul_f32_e32 v139, 0x42800000, v33
	v_cvt_pk_fp8_f32 v137, v138, v139 op_sel:[0,0,1]
	ds_write_b64 v238, v[136:137] offset:384
	s_cbranch_vccnz .LBB0_170
	v_lshl_or_b32 v32, s4, 7, v1
	v_or_b32_e32 v2, 39, v32
	v_mul_u32_u24_e32 v4, s26, v2
	v_lshlrev_b32_e32 v2, 2, v4
	v_mov_b32_e32 v3, v131
	s_lshl_b32 s16, s24, 8
	s_mov_b32 s17, s9
	v_lshl_add_u64 v[2:3], s[12:13], 0, v[2:3]
	s_lshl_b64 s[16:17], s[16:17], 2
	v_lshl_add_u64 v[2:3], v[2:3], 0, s[16:17]
	v_lshl_add_u64 v[30:31], v[2:3], 0, v[130:131]
	v_subrev_u32_e32 v2, s26, v4
	v_mov_b32_e32 v3, v131
	v_lshl_add_u64 v[4:5], v[2:3], 2, s[12:13]
	v_lshl_add_u64 v[4:5], v[4:5], 0, s[16:17]
	v_subrev_u32_e32 v2, s26, v2
	v_lshl_add_u64 v[26:27], v[4:5], 0, v[130:131]
	v_lshl_add_u64 v[4:5], v[2:3], 2, s[12:13]
	v_lshl_add_u64 v[4:5], v[4:5], 0, s[16:17]
	v_subrev_u32_e32 v2, s26, v2
	v_lshl_add_u64 v[22:23], v[4:5], 0, v[130:131]
	v_lshl_add_u64 v[4:5], v[2:3], 2, s[12:13]
	v_lshl_add_u64 v[4:5], v[4:5], 0, s[16:17]
	v_subrev_u32_e32 v2, s26, v2
	v_lshl_add_u64 v[18:19], v[4:5], 0, v[130:131]
	v_lshl_add_u64 v[4:5], v[2:3], 2, s[12:13]
	v_lshl_add_u64 v[4:5], v[4:5], 0, s[16:17]
	v_subrev_u32_e32 v2, s26, v2
	v_lshl_add_u64 v[14:15], v[4:5], 0, v[130:131]
	v_lshl_add_u64 v[4:5], v[2:3], 2, s[12:13]
	v_lshl_add_u64 v[4:5], v[4:5], 0, s[16:17]
	v_subrev_u32_e32 v2, s26, v2
	v_lshl_add_u64 v[10:11], v[4:5], 0, v[130:131]
	v_lshl_add_u64 v[4:5], v[2:3], 2, s[12:13]
	v_lshl_add_u64 v[4:5], v[4:5], 0, s[16:17]
	v_subrev_u32_e32 v2, s26, v2
	s_mul_i32 s5, s26, 0xffffffe7
	v_lshl_add_u64 v[6:7], v[4:5], 0, v[130:131]
	v_lshl_add_u64 v[4:5], v[2:3], 2, s[12:13]
	v_add_u32_e32 v2, s5, v2
	v_lshl_add_u64 v[8:9], v[2:3], 2, s[12:13]
	v_subrev_u32_e32 v2, s26, v2
	v_lshl_add_u64 v[12:13], v[2:3], 2, s[12:13]
	v_subrev_u32_e32 v2, s26, v2
	v_lshl_add_u64 v[16:17], v[2:3], 2, s[12:13]
	v_subrev_u32_e32 v2, s26, v2
	v_lshl_add_u64 v[20:21], v[2:3], 2, s[12:13]
	v_subrev_u32_e32 v2, s26, v2
	v_lshl_add_u64 v[24:25], v[2:3], 2, s[12:13]
	v_subrev_u32_e32 v2, s26, v2
	v_mul_u32_u24_e32 v32, s26, v32
	v_lshl_add_u64 v[28:29], v[2:3], 2, s[12:13]
	v_subrev_u32_e32 v2, s26, v2
	v_lshlrev_b32_e32 v32, 2, v32
	v_mov_b32_e32 v33, v131
	v_lshl_add_u64 v[2:3], v[2:3], 2, s[12:13]
	v_lshl_add_u64 v[32:33], s[12:13], 0, v[32:33]
	v_lshl_add_u64 v[4:5], v[4:5], 0, s[16:17]
	v_lshl_add_u64 v[8:9], v[8:9], 0, s[16:17]
	v_lshl_add_u64 v[12:13], v[12:13], 0, s[16:17]
	v_lshl_add_u64 v[16:17], v[16:17], 0, s[16:17]
	v_lshl_add_u64 v[20:21], v[20:21], 0, s[16:17]
	v_lshl_add_u64 v[24:25], v[24:25], 0, s[16:17]
	v_lshl_add_u64 v[28:29], v[28:29], 0, s[16:17]
	v_lshl_add_u64 v[2:3], v[2:3], 0, s[16:17]
	v_lshl_add_u64 v[32:33], v[32:33], 0, s[16:17]
	v_lshl_add_u64 v[4:5], v[4:5], 0, v[130:131]
	v_lshl_add_u64 v[8:9], v[8:9], 0, v[130:131]
	v_lshl_add_u64 v[12:13], v[12:13], 0, v[130:131]
	v_lshl_add_u64 v[16:17], v[16:17], 0, v[130:131]
	v_lshl_add_u64 v[20:21], v[20:21], 0, v[130:131]
	v_lshl_add_u64 v[24:25], v[24:25], 0, v[130:131]
	v_lshl_add_u64 v[28:29], v[28:29], 0, v[130:131]
	v_lshl_add_u64 v[2:3], v[2:3], 0, v[130:131]
	v_lshl_add_u64 v[32:33], v[32:33], 0, v[130:131]
	global_load_dwordx4 v[58:61], v[32:33], off nt
	global_load_dwordx4 v[62:65], v[2:3], off nt
	global_load_dwordx4 v[50:53], v[28:29], off nt
	global_load_dwordx4 v[42:45], v[24:25], off nt
	global_load_dwordx4 v[54:57], v[20:21], off nt
	global_load_dwordx4 v[34:37], v[16:17], off nt
	global_load_dwordx4 v[38:41], v[12:13], off nt
	global_load_dwordx4 v[46:49], v[8:9], off nt
	s_nop 0
	global_load_dwordx4 v[2:5], v[4:5], off nt
	s_nop 0
	global_load_dwordx4 v[6:9], v[6:7], off nt
	s_nop 0
	global_load_dwordx4 v[10:13], v[10:11], off nt
	s_nop 0
	global_load_dwordx4 v[14:17], v[14:15], off nt
	s_nop 0
	global_load_dwordx4 v[18:21], v[18:19], off nt
	s_nop 0
	global_load_dwordx4 v[22:25], v[22:23], off nt
	s_nop 0
	global_load_dwordx4 v[26:29], v[26:27], off nt
	s_nop 0
	global_load_dwordx4 v[30:33], v[30:31], off nt
	s_branch .LBB0_170
